# diff attention near-diagonal tiles: straight-line bias lookup and causal mask instead of 32 predicated LDS round trips
# baseline (speedup 1.0000x reference)
.LBB0_634:
	s_or_b64 exec, exec, s[0:1]
	v_mov_b32_e32 v1, 0
	ds_write_b32 v217, v1 offset:512
	s_not_b32 s0, s9
	s_bfe_u32 s73, s2, 0x20006
	s_lshl_b32 s0, s0, 7
	s_ashr_i32 s10, s5, 3
	s_and_b32 s53, s0, 0x1f80
	s_lshl_b32 s0, s73, 5
	s_or_b32 s9, s0, s53
	s_and_b32 s0, s2, 0x3fffffc0
	s_ashr_i32 s11, s10, 31
	v_or_b32_e32 v1, s9, v180
	s_lshl_b32 s0, s0, 2
	s_lshl_b64 s[54:55], s[10:11], 13
	s_add_i32 s95, s0, 0
	v_or_b32_e32 v1, s54, v1
	v_mov_b64_e32 v[4:5], s[88:89]
	s_movk_i32 s0, 0x6880
	v_mad_u64_u32 v[4:5], s[0:1], v1, s0, v[4:5]
	s_lshr_b32 s13, s2, 8
	v_mad_i32_i24 v5, s55, v227, v5
	s_lshl_b32 s42, s4, 8
	v_lshl_add_u64 v[4:5], v[4:5], 0, s[42:43]
	s_lshl_b32 s0, s13, 7
	s_mov_b32 s1, s43
	s_lshr_b32 s12, s2, 6
	s_add_i32 s95, s95, 0x20800
	s_lshl_b32 s72, s4, 7
	v_lshl_add_u64 v[4:5], v[4:5], 0, s[0:1]
	s_mul_i32 s1, s10, 0xd100000
	s_mul_hi_i32 s14, s10, 0xd100000
	s_add_u32 s4, s88, s1
	s_addc_u32 s5, s89, s14
	s_add_u32 s4, s4, s42
	s_addc_u32 s5, s5, 0
	s_lshl_b32 s15, s12, 3
	s_lshr_b32 s10, s2, 4
	v_or_b32_e32 v6, s15, v193
	s_and_b32 s16, s10, 4
	v_mad_u64_u32 v[6:7], s[10:11], v6, s94, v[200:201]
	v_or_b32_e32 v7, s15, v221
	v_bitop3_b32 v1, s15, v228, v218 bitop3:0xc8
	v_mad_u64_u32 v[8:9], s[10:11], v7, s94, v[202:203]
	v_mov_b32_e32 v7, v3
	v_or3_b32 v2, v219, v1, s16
	s_lshl_b32 s10, s12, 11
	v_lshlrev_b64 v[6:7], 1, v[6:7]
	v_mul_lo_u32 v2, v2, s94
	v_lshl_add_u64 v[12:13], s[4:5], 0, v[6:7]
	s_mov_b64 s[18:19], 0x800
	s_add_i32 s52, s10, 0
	v_or_b32_e32 v2, v2, v223
	v_lshl_add_u64 v[12:13], v[12:13], 0, s[18:19]
	s_mov_b32 m0, s52
	s_mov_b64 s[10:11], 0x1000
	global_load_lds_dwordx4 v[12:13], off
	v_lshlrev_b64 v[12:13], 1, v[2:3]
	v_lshl_add_u64 v[14:15], s[4:5], 0, v[12:13]
	v_mov_b32_e32 v9, v3
	v_lshl_add_u64 v[16:17], v[14:15], 0, s[10:11]
	s_add_i32 m0, s52, 0x4000
	v_lshlrev_b64 v[8:9], 1, v[8:9]
	global_load_lds_dwordx4 v[16:17], off
	v_lshl_add_u64 v[16:17], s[4:5], 0, v[8:9]
	v_lshl_add_u64 v[16:17], v[16:17], 0, s[18:19]
	s_add_i32 m0, s52, 0x400
	s_addk_i32 s53, 0x80
	global_load_lds_dwordx4 v[16:17], off
	s_mov_b64 s[10:11], 0x1080
	s_add_i32 m0, s52, 0x4400
	v_lshl_add_u64 v[14:15], v[14:15], 0, s[10:11]
	s_add_u32 s10, s4, 0x1a2800
	s_addc_u32 s11, s5, 0
	s_add_u32 s4, s4, 0x1a3000
	global_load_lds_dwordx4 v[14:15], off
	s_addc_u32 s5, s5, 0
	v_lshl_add_u64 v[6:7], s[10:11], 0, v[6:7]
	s_add_i32 m0, s52, 0x8000
	v_add_u32_e32 v10, 64, v2
	global_load_lds_dwordx4 v[6:7], off
	v_lshl_add_u64 v[6:7], s[4:5], 0, v[12:13]
	s_add_i32 m0, s52, 0xc000
	v_mov_b32_e32 v11, v3
	global_load_lds_dwordx4 v[6:7], off
	v_lshl_add_u64 v[6:7], s[10:11], 0, v[8:9]
	s_add_i32 m0, s52, 0x8400
	v_lshlrev_b32_e32 v2, 1, v182
	global_load_lds_dwordx4 v[6:7], off
	v_lshl_add_u64 v[6:7], v[10:11], 1, s[4:5]
	s_add_i32 m0, s52, 0xc400
	v_lshl_add_u64 v[4:5], v[4:5], 0, v[2:3]
	global_load_lds_dwordx4 v[6:7], off
	global_load_dwordx4 v[132:135], v[4:5], off
	global_load_dwordx4 v[136:139], v[4:5], off offset:32
	global_load_dwordx4 v[140:143], v[4:5], off offset:64
	global_load_dwordx4 v[144:147], v[4:5], off offset:96
	s_lshr_b32 s76, s53, 6
	s_cmp_eq_u32 s13, 1
	s_cselect_b64 s[56:57], -1, 0
	s_cmpk_lt_u32 s2, 0x100
	v_or_b32_e32 v2, s0, v183
	s_cselect_b64 s[58:59], -1, 0
	v_bitop3_b32 v234, s0, v186, v183 bitop3:0x36
	s_movk_i32 s0, 0x60
	s_sub_i32 s77, 0xb0, s9
	s_or_b32 s2, s1, s42
	v_add3_u32 v1, v219, v1, s16
	v_bitop3_b32 v237, v2, v186, s0 bitop3:0x36
	v_mul_lo_u32 v1, v1, s94
	s_add_u32 s0, s92, s2
	v_bitop3_b32 v235, v2, v186, 32 bitop3:0x36
	v_bitop3_b32 v236, v2, v186, 64 bitop3:0x36
	v_or_b32_e32 v2, v223, v1
	s_addc_u32 s1, s93, s14
	v_lshl_add_u64 v[206:207], v[2:3], 1, s[0:1]
	s_mul_i32 s12, s12, 0x1a200
	s_add_u32 s0, s84, s2
	v_add_u32_e32 v2, s12, v224
	s_addc_u32 s1, s97, s14
	v_lshl_add_u64 v[208:209], v[2:3], 1, s[0:1]
	v_add_u32_e32 v2, s12, v225
	v_mov_b32_e32 v16, v3
	v_mov_b32_e32 v17, v3
	v_lshl_add_u64 v[210:211], v[2:3], 1, s[0:1]
	v_mov_b32_e32 v2, v3
	v_mov_b32_e32 v4, v3
	v_mov_b32_e32 v5, v3
	v_mov_b32_e32 v6, v3
	v_mov_b32_e32 v7, v3
	v_mov_b32_e32 v8, v3
	v_mov_b32_e32 v9, v3
	v_mov_b32_e32 v10, v3
	v_mov_b32_e32 v12, v3
	v_mov_b32_e32 v13, v3
	v_mov_b32_e32 v14, v3
	v_mov_b32_e32 v15, v3
	v_mov_b64_e32 v[66:67], v[16:17]
	v_mov_b64_e32 v[50:51], v[16:17]
	v_mov_b64_e32 v[34:35], v[16:17]
	v_mov_b64_e32 v[64:65], v[14:15]
	v_mov_b64_e32 v[62:63], v[12:13]
	v_mov_b64_e32 v[60:61], v[10:11]
	v_mov_b64_e32 v[58:59], v[8:9]
	v_mov_b64_e32 v[56:57], v[6:7]
	v_mov_b64_e32 v[54:55], v[4:5]
	v_mov_b64_e32 v[52:53], v[2:3]
	v_mov_b64_e32 v[48:49], v[14:15]
	v_mov_b64_e32 v[46:47], v[12:13]
	v_mov_b64_e32 v[44:45], v[10:11]
	v_mov_b64_e32 v[42:43], v[8:9]
	v_mov_b64_e32 v[40:41], v[6:7]
	v_mov_b64_e32 v[38:39], v[4:5]
	v_mov_b64_e32 v[36:37], v[2:3]
	v_mov_b64_e32 v[32:33], v[14:15]
	v_mov_b64_e32 v[30:31], v[12:13]
	v_mov_b64_e32 v[28:29], v[10:11]
	v_mov_b64_e32 v[26:27], v[8:9]
	v_mov_b64_e32 v[24:25], v[6:7]
	v_mov_b64_e32 v[22:23], v[4:5]
	v_mov_b64_e32 v[20:21], v[2:3]
	v_mov_b64_e32 v[18:19], v[16:17]
	s_mov_b32 s68, 2
	v_mov_b32_e32 v69, v68
	v_mov_b32_e32 v70, v68
	v_mov_b32_e32 v71, v68
	v_mov_b32_e32 v72, v68
	v_mov_b32_e32 v73, v68
	v_mov_b32_e32 v74, v68
	v_mov_b32_e32 v75, v68
	v_mov_b32_e32 v76, v68
	v_mov_b32_e32 v77, v68
	v_mov_b32_e32 v78, v68
	v_mov_b32_e32 v79, v68
	v_mov_b32_e32 v80, v68
	v_mov_b32_e32 v81, v68
	v_mov_b32_e32 v82, v68
	v_mov_b32_e32 v83, v68
	v_lshl_add_u32 v232, v180, 2, s95
	v_add_u32_e32 v238, s9, v226
	s_mov_b32 s42, 0
	v_mov_b32_e32 v233, 0
	s_mov_b32 s4, 0x10000
	s_mov_b64 s[60:61], 0
	v_mov_b32_e32 v84, 0
	v_mov_b32_e32 v85, 0
	v_mov_b32_e32 v86, 0
	v_mov_b32_e32 v87, 0
	v_mov_b32_e32 v88, 0
	v_mov_b32_e32 v89, 0
	v_mov_b32_e32 v90, 0
	v_mov_b32_e32 v91, 0
	v_mov_b32_e32 v92, 0
	v_mov_b32_e32 v93, 0
	v_mov_b32_e32 v94, 0
	v_mov_b32_e32 v95, 0
	v_mov_b32_e32 v96, 0
	v_mov_b32_e32 v97, 0
	v_mov_b32_e32 v98, 0
	v_mov_b32_e32 v99, 0
	v_mov_b64_e32 v[16:17], v[14:15]
	v_mov_b64_e32 v[14:15], v[12:13]
	v_mov_b64_e32 v[12:13], v[10:11]
	v_mov_b64_e32 v[10:11], v[8:9]
	v_mov_b64_e32 v[8:9], v[6:7]
	v_mov_b64_e32 v[6:7], v[4:5]
	v_mov_b64_e32 v[4:5], v[2:3]
	s_waitcnt vmcnt(0)
	s_branch .LBB0_636

.LBB0_642:
	s_add_i32 s0, s4, 0xffff0000
	s_and_b32 s2, s0, 0x18000
	v_add_u32_e32 v1, s2, v185
	v_add_u32_e32 v2, v1, v234
	ds_read_b128 v[148:151], v2
	ds_read_b128 v[152:155], v2 offset:8192
	v_add_u32_e32 v2, v1, v235
	ds_read_b128 v[156:159], v2
	ds_read_b128 v[160:163], v2 offset:8192
	v_add_u32_e32 v2, v1, v236
	s_waitcnt lgkmcnt(0)
	v_mfma_f32_32x32x16_bf16 v[100:115], v[148:151], v[132:135], v[68:83]
	ds_read_b128 v[164:167], v2
	ds_read_b128 v[168:171], v2 offset:8192
	v_add_u32_e32 v1, v1, v237
	ds_read_b128 v[176:179], v1
	ds_read_b128 v[172:175], v1 offset:8192
	s_cmp_lt_i32 s42, s77
	s_cselect_b64 s[64:65], -1, 0
	s_cmp_ge_i32 s42, s77
	v_mfma_f32_32x32x16_bf16 v[84:99], v[152:155], v[132:135], v[68:83]
	v_mfma_f32_32x32x16_bf16 v[100:115], v[156:159], v[136:139], v[100:115]
	v_mfma_f32_32x32x16_bf16 v[84:99], v[160:163], v[136:139], v[84:99]
	s_waitcnt lgkmcnt(0)
	v_mfma_f32_32x32x16_bf16 v[100:115], v[164:167], v[140:143], v[100:115]
	s_waitcnt lgkmcnt(2)
	v_mfma_f32_32x32x16_bf16 v[84:99], v[168:171], v[140:143], v[84:99]
	s_waitcnt lgkmcnt(1)
	v_mfma_f32_32x32x16_bf16 v[100:115], v[176:179], v[144:147], v[100:115]
	s_waitcnt lgkmcnt(0)
	v_mfma_f32_32x32x16_bf16 v[84:99], v[172:175], v[144:147], v[84:99]
	s_cbranch_scc1 .LBB0_676
	v_add_u32_e32 v239, s42, v238
	v_lshlrev_b32_e32 v1, 2, v239
	v_add_u32_e32 v1, 0x20f14, v1
	ds_read_b32 v116, v1 offset:236
	ds_read_b32 v117, v1 offset:232
	ds_read_b32 v118, v1 offset:228
	ds_read_b32 v119, v1 offset:224
	ds_read_b32 v120, v1 offset:204
	ds_read_b32 v121, v1 offset:200
	ds_read_b32 v122, v1 offset:196
	ds_read_b32 v123, v1 offset:192
	ds_read_b32 v124, v1 offset:172
	ds_read_b32 v125, v1 offset:168
	ds_read_b32 v126, v1 offset:164
	ds_read_b32 v127, v1 offset:160
	ds_read_b32 v128, v1 offset:140
	ds_read_b32 v129, v1 offset:136
	ds_read_b32 v130, v1 offset:132
	ds_read_b32 v131, v1 offset:128
	v_cmp_gt_i32_e64 s[10:11], 0, v239
	v_cmp_gt_i32_e64 s[12:13], 1, v239
	v_cmp_gt_i32_e64 s[14:15], 2, v239
	v_cmp_gt_i32_e64 s[16:17], 3, v239
	v_cmp_gt_i32_e64 s[18:19], 8, v239
	v_cmp_gt_i32_e64 s[20:21], 9, v239
	v_cmp_gt_i32_e64 s[22:23], 10, v239
	v_cmp_gt_i32_e64 s[24:25], 11, v239
	v_cmp_gt_i32_e64 s[26:27], 16, v239
	v_cmp_gt_i32_e64 s[28:29], 17, v239
	v_cmp_gt_i32_e64 s[30:31], 18, v239
	v_cmp_gt_i32_e64 s[32:33], 19, v239
	v_cmp_gt_i32_e64 s[34:35], 24, v239
	v_cmp_gt_i32_e64 s[36:37], 25, v239
	v_cmp_gt_i32_e64 s[38:39], 26, v239
	v_cmp_gt_i32_e64 s[40:41], 27, v239
	s_waitcnt lgkmcnt(15)
	v_add_f32_e32 v100, v100, v116
	s_waitcnt lgkmcnt(14)
	v_add_f32_e32 v101, v101, v117
	s_waitcnt lgkmcnt(13)
	v_add_f32_e32 v102, v102, v118
	s_waitcnt lgkmcnt(12)
	v_add_f32_e32 v103, v103, v119
	s_waitcnt lgkmcnt(11)
	v_add_f32_e32 v104, v104, v120
	s_waitcnt lgkmcnt(10)
	v_add_f32_e32 v105, v105, v121
	s_waitcnt lgkmcnt(9)
	v_add_f32_e32 v106, v106, v122
	s_waitcnt lgkmcnt(8)
	v_add_f32_e32 v107, v107, v123
	s_waitcnt lgkmcnt(7)
	v_add_f32_e32 v108, v108, v124
	s_waitcnt lgkmcnt(6)
	v_add_f32_e32 v109, v109, v125
	s_waitcnt lgkmcnt(5)
	v_add_f32_e32 v110, v110, v126
	s_waitcnt lgkmcnt(4)
	v_add_f32_e32 v111, v111, v127
	s_waitcnt lgkmcnt(3)
	v_add_f32_e32 v112, v112, v128
	s_waitcnt lgkmcnt(2)
	v_add_f32_e32 v113, v113, v129
	s_waitcnt lgkmcnt(1)
	v_add_f32_e32 v114, v114, v130
	s_waitcnt lgkmcnt(0)
	v_add_f32_e32 v115, v115, v131
	ds_read_b32 v116, v1 offset:108
	ds_read_b32 v117, v1 offset:104
	ds_read_b32 v118, v1 offset:100
	ds_read_b32 v119, v1 offset:96
	ds_read_b32 v120, v1 offset:76
	ds_read_b32 v121, v1 offset:72
	ds_read_b32 v122, v1 offset:68
	ds_read_b32 v123, v1 offset:64
	ds_read_b32 v124, v1 offset:44
	ds_read_b32 v125, v1 offset:40
	ds_read_b32 v126, v1 offset:36
	ds_read_b32 v127, v1 offset:32
	ds_read_b32 v128, v1 offset:12
	ds_read_b32 v129, v1 offset:8
	ds_read_b32 v130, v1 offset:4
	ds_read_b32 v131, v1 offset:0
	v_cndmask_b32_e64 v100, v100, v229, s[10:11]
	v_cndmask_b32_e64 v101, v101, v229, s[12:13]
	v_cndmask_b32_e64 v102, v102, v229, s[14:15]
	v_cndmask_b32_e64 v103, v103, v229, s[16:17]
	v_cndmask_b32_e64 v104, v104, v229, s[18:19]
	v_cndmask_b32_e64 v105, v105, v229, s[20:21]
	v_cndmask_b32_e64 v106, v106, v229, s[22:23]
	v_cndmask_b32_e64 v107, v107, v229, s[24:25]
	v_cndmask_b32_e64 v108, v108, v229, s[26:27]
	v_cndmask_b32_e64 v109, v109, v229, s[28:29]
	v_cndmask_b32_e64 v110, v110, v229, s[30:31]
	v_cndmask_b32_e64 v111, v111, v229, s[32:33]
	v_cndmask_b32_e64 v112, v112, v229, s[34:35]
	v_cndmask_b32_e64 v113, v113, v229, s[36:37]
	v_cndmask_b32_e64 v114, v114, v229, s[38:39]
	v_cndmask_b32_e64 v115, v115, v229, s[40:41]
	v_cmp_gt_i32_e64 s[10:11], 32, v239
	v_cmp_gt_i32_e64 s[12:13], 33, v239
	v_cmp_gt_i32_e64 s[14:15], 34, v239
	v_cmp_gt_i32_e64 s[16:17], 35, v239
	v_cmp_gt_i32_e64 s[18:19], 40, v239
	v_cmp_gt_i32_e64 s[20:21], 41, v239
	v_cmp_gt_i32_e64 s[22:23], 42, v239
	v_cmp_gt_i32_e64 s[24:25], 43, v239
	v_cmp_gt_i32_e64 s[26:27], 48, v239
	v_cmp_gt_i32_e64 s[28:29], 49, v239
	v_cmp_gt_i32_e64 s[30:31], 50, v239
	v_cmp_gt_i32_e64 s[32:33], 51, v239
	v_cmp_gt_i32_e64 s[34:35], 56, v239
	v_cmp_gt_i32_e64 s[36:37], 57, v239
	v_cmp_gt_i32_e64 s[38:39], 58, v239
	v_cmp_gt_i32_e64 s[40:41], 59, v239
	s_waitcnt lgkmcnt(15)
	v_add_f32_e32 v84, v84, v116
	s_waitcnt lgkmcnt(14)
	v_add_f32_e32 v85, v85, v117
	s_waitcnt lgkmcnt(13)
	v_add_f32_e32 v86, v86, v118
	s_waitcnt lgkmcnt(12)
	v_add_f32_e32 v87, v87, v119
	s_waitcnt lgkmcnt(11)
	v_add_f32_e32 v88, v88, v120
	s_waitcnt lgkmcnt(10)
	v_add_f32_e32 v89, v89, v121
	s_waitcnt lgkmcnt(9)
	v_add_f32_e32 v90, v90, v122
	s_waitcnt lgkmcnt(8)
	v_add_f32_e32 v91, v91, v123
	s_waitcnt lgkmcnt(7)
	v_add_f32_e32 v92, v92, v124
	s_waitcnt lgkmcnt(6)
	v_add_f32_e32 v93, v93, v125
	s_waitcnt lgkmcnt(5)
	v_add_f32_e32 v94, v94, v126
	s_waitcnt lgkmcnt(4)
	v_add_f32_e32 v95, v95, v127
	s_waitcnt lgkmcnt(3)
	v_add_f32_e32 v96, v96, v128
	s_waitcnt lgkmcnt(2)
	v_add_f32_e32 v97, v97, v129
	s_waitcnt lgkmcnt(1)
	v_add_f32_e32 v98, v98, v130
	s_waitcnt lgkmcnt(0)
	v_add_f32_e32 v99, v99, v131
	v_cndmask_b32_e64 v84, v84, v229, s[10:11]
	v_cndmask_b32_e64 v85, v85, v229, s[12:13]
	v_cndmask_b32_e64 v86, v86, v229, s[14:15]
	v_cndmask_b32_e64 v87, v87, v229, s[16:17]
	v_cndmask_b32_e64 v88, v88, v229, s[18:19]
	v_cndmask_b32_e64 v89, v89, v229, s[20:21]
	v_cndmask_b32_e64 v90, v90, v229, s[22:23]
	v_cndmask_b32_e64 v91, v91, v229, s[24:25]
	v_cndmask_b32_e64 v92, v92, v229, s[26:27]
	v_cndmask_b32_e64 v93, v93, v229, s[28:29]
	v_cndmask_b32_e64 v94, v94, v229, s[30:31]
	v_cndmask_b32_e64 v95, v95, v229, s[32:33]
	v_cndmask_b32_e64 v96, v96, v229, s[34:35]
	v_cndmask_b32_e64 v97, v97, v229, s[36:37]
	v_cndmask_b32_e64 v98, v98, v229, s[38:39]
	v_cndmask_b32_e64 v99, v99, v229, s[40:41]
